# v56 + the last 256 items of every PEER gather queue are split into 4-token halves (shorter end-of-phase tail)
# speedup vs baseline: 1.0180x; 1.0048x over previous
.LBB0_1982:
	v_readfirstlane_b32 s24, v91
	s_lshr_b32 s6, s32, 15
	s_add_i32 s24, s24, s6
	s_cmpk_lt_u32 s24, 0x1100
	s_cbranch_scc1 .LBB0_1989
	s_add_i32 s6, s20, s17
	s_lshl_b32 s14, s6, 6
	s_branch .LBB0_1986

.LBB0_1994:
	s_lshl_b32 s25, s26, 3
	s_and_b32 s25, s25, 0x3ff8
	s_lshr_b32 s13, s26, 11
	s_lshl_b32 s24, s26, 2
	s_add_i32 s24, s24, 0xfffffc00
	s_cmp_ge_u32 s26, 0xf00
	s_cselect_b32 s25, s24, s25
	s_cselect_b32 s13, 1, s13
	s_cselect_b32 s46, 4, 8
	s_add_i32 s45, s46, -2
	s_lshl_b32 s12, s23, 1
	s_add_i32 s94, s12, s13
	s_xor_b64 s[6:7], s[14:15], -1
	s_lshl_b64 s[12:13], s[94:95], 21
	s_add_u32 s12, s18, s12
	s_addc_u32 s13, s19, s13
	s_lshl_b32 s24, s21, 3
	s_and_b32 s24, s24, 0x3ff8
	s_lshr_b32 s44, s21, 11
	s_lshl_b32 s26, s21, 2
	s_add_i32 s26, s26, 0xfffffc00
	s_cmp_ge_u32 s21, 0xf00
	s_cselect_b32 s24, s26, s24
	s_cselect_b32 s44, 1, s44
	s_lshl_b32 s23, s22, 1
	s_add_i32 s23, s44, s23
	s_and_b64 s[48:49], s[14:15], exec
	s_cselect_b32 s23, s23, s94
	s_cselect_b32 s14, s24, s25
	s_or_b32 s24, s25, 2
	s_sub_i32 s44, s14, s45
	s_lshl_b64 s[14:15], s[94:95], 22
	s_lshl_b32 s26, s25, 8
	s_or_b32 s14, s14, s26
	v_readlane_b32 s0, v255, 35
	v_readlane_b32 s1, v255, 36
	s_mov_b32 s25, s44
	s_add_u32 s14, s0, s14
	s_addc_u32 s15, s1, s15
	s_mov_b32 s26, 0
	v_readlane_b32 s0, v253, 59
.LBB0_1995:
	v_mov_b32_e32 v94, v90
	s_waitcnt lgkmcnt(0)
	v_mov_b64_e32 v[22:23], v[18:19]
	v_mov_b64_e32 v[20:21], v[16:17]
	v_and_b32_e32 v93, 7, v94
	v_lshlrev_b32_e32 v16, 4, v93
	v_add_u32_e32 v12, v16, v12
	v_add_u32_e32 v8, v16, v8
	global_load_dwordx4 v[84:87], v12, s[12:13]
	global_load_dwordx4 v[68:71], v8, s[12:13]
	v_add_u32_e32 v12, v16, v13
	v_add_u32_e32 v8, v16, v9
	global_load_dwordx4 v[80:83], v12, s[12:13]
	global_load_dwordx4 v[64:67], v8, s[12:13]
	v_add_u32_e32 v12, v16, v14
	v_add_u32_e32 v8, v16, v10
	global_load_dwordx4 v[76:79], v12, s[12:13]
	global_load_dwordx4 v[60:63], v8, s[12:13]
	v_add_u32_e32 v12, v16, v15
	global_load_dwordx4 v[72:75], v12, s[12:13]
	v_add_u32_e32 v8, v16, v11
	global_load_dwordx4 v[56:59], v8, s[12:13]
	v_add_u32_e32 v4, v16, v4
	v_add_u32_e32 v0, v16, v0
	global_load_dwordx4 v[52:55], v4, s[12:13]
	global_load_dwordx4 v[36:39], v0, s[12:13]
	v_add_u32_e32 v4, v16, v5
	v_add_u32_e32 v0, v16, v1
	global_load_dwordx4 v[48:51], v4, s[12:13]
	global_load_dwordx4 v[32:35], v0, s[12:13]
	v_add_u32_e32 v4, v16, v6
	v_add_u32_e32 v0, v16, v2
	global_load_dwordx4 v[44:47], v4, s[12:13]
	global_load_dwordx4 v[28:31], v0, s[12:13]
	v_add_u32_e32 v4, v16, v7
	global_load_dwordx4 v[40:43], v4, s[12:13]
	v_add_u32_e32 v0, v16, v3
	global_load_dwordx4 v[24:27], v0, s[12:13]
	v_lshl_add_u32 v0, v94, 3, s84
	s_waitcnt vmcnt(17)
	ds_write_b64 v0, v[88:89]
	v_mad_u64_u32 v[0:1], s[28:29], v94, -6, v[0:1]
	s_cmp_lt_u32 s26, s45
	s_cselect_b32 s28, s24, s25
	s_cselect_b32 s27, s94, s23
	s_add_i32 s28, s28, s26
	s_ashr_i32 s29, s28, 31
	s_lshl_b64 s[30:31], s[28:29], 9
	s_add_u32 s30, s82, s30
	s_addc_u32 s31, s83, s31
	s_lshl_b64 s[28:29], s[28:29], 11
	s_add_u32 s28, s85, s28
	s_addc_u32 s29, s0, s29
	s_lshl_b32 s27, s27, 7
	v_lshlrev_b32_e32 v96, 1, v94
	s_add_u32 s28, s28, s27
	v_ashrrev_i32_e32 v95, 3, v94
	s_waitcnt vmcnt(16)
	ds_write_b16 v0, v92 offset:512
	v_ashrrev_i32_e32 v97, 31, v96
	s_addc_u32 s29, s29, 0
	s_waitcnt lgkmcnt(0)
	v_lshl_add_u32 v0, v95, 6, s84
	v_lshl_add_u64 v[88:89], v[96:97], 2, s[30:31]
	v_lshl_add_u64 v[96:97], s[28:29], 0, v[96:97]
	ds_read_b128 v[12:15], v0
	ds_read_b128 v[8:11], v0 offset:16
	ds_read_b128 v[4:7], v0 offset:32
	ds_read_b128 v[0:3], v0 offset:48
	global_load_dwordx2 v[88:89], v[88:89], off
	s_mov_b32 s27, 0xffff
	global_load_ushort v92, v[96:97], off
	v_mov_b32_e32 v96, 0
	v_add_u32_e32 v16, s84, v16
	ds_read_b128 v[16:19], v16 offset:512
	s_add_i32 s26, s26, 1
	s_waitcnt vmcnt(17)
	v_dot4c_i32_i8_e32 v96, v84, v20
	v_mov_b32_e32 v84, 0
	v_dot4c_i32_i8_e32 v96, v85, v21
	v_dot4c_i32_i8_e32 v96, v86, v22
	s_waitcnt vmcnt(15)
	v_dot4c_i32_i8_e32 v84, v80, v20
	v_mov_b32_e32 v80, 0
	v_dot4c_i32_i8_e32 v84, v81, v21
	v_dot4c_i32_i8_e32 v96, v87, v23
	s_waitcnt vmcnt(13)
	v_dot4c_i32_i8_e32 v80, v76, v20
	v_mov_b32_e32 v76, 0
	v_dot4c_i32_i8_e32 v84, v82, v22
	s_waitcnt vmcnt(11)
	v_dot4c_i32_i8_e32 v76, v72, v20
	v_mov_b32_e32 v72, 0
	v_dot4c_i32_i8_e32 v72, v68, v20
	v_mov_b32_e32 v68, 0
	v_dot4c_i32_i8_e32 v68, v64, v20
	v_mov_b32_e32 v64, 0
	v_dot4c_i32_i8_e32 v64, v60, v20
	v_mov_b32_e32 v60, 0
	s_waitcnt vmcnt(10)
	v_dot4c_i32_i8_e32 v60, v56, v20
	v_mov_b32_e32 v56, 0
	s_waitcnt vmcnt(9)
	v_dot4c_i32_i8_e32 v56, v52, v20
	v_mov_b32_e32 v52, 0
	s_waitcnt vmcnt(7)
	v_dot4c_i32_i8_e32 v52, v48, v20
	v_mov_b32_e32 v48, 0
	s_waitcnt vmcnt(5)
	v_dot4c_i32_i8_e32 v48, v44, v20
	v_mov_b32_e32 v44, 0
	s_waitcnt vmcnt(3)
	v_dot4c_i32_i8_e32 v44, v40, v20
	v_mov_b32_e32 v40, 0
	v_dot4c_i32_i8_e32 v40, v36, v20
	v_mov_b32_e32 v36, 0
	v_dot4c_i32_i8_e32 v36, v32, v20
	v_mov_b32_e32 v32, 0
	v_dot4c_i32_i8_e32 v56, v53, v21
	v_dot4c_i32_i8_e32 v32, v28, v20
	v_mov_b32_e32 v28, 0
	v_dot4c_i32_i8_e32 v56, v54, v22
	v_dot4c_i32_i8_e32 v52, v49, v21
	s_waitcnt vmcnt(2)
	v_dot4c_i32_i8_e32 v28, v24, v20
	v_and_b32_e32 v20, 4, v94
	v_dot4c_i32_i8_e32 v80, v77, v21
	v_dot4c_i32_i8_e32 v56, v55, v23
	v_dot4c_i32_i8_e32 v52, v50, v22
	v_dot4c_i32_i8_e32 v48, v45, v21
	v_cmp_eq_u32_e32 vcc, 0, v20
	v_dot4c_i32_i8_e32 v84, v83, v23
	v_dot4c_i32_i8_e32 v80, v78, v22
	v_dot4c_i32_i8_e32 v76, v73, v21
	v_dot4c_i32_i8_e32 v72, v69, v21
	v_dot4c_i32_i8_e32 v68, v65, v21
	v_dot4c_i32_i8_e32 v64, v61, v21
	v_dot4c_i32_i8_e32 v60, v57, v21
	v_dot4c_i32_i8_e32 v52, v51, v23
	v_dot4c_i32_i8_e32 v48, v46, v22
	v_dot4c_i32_i8_e32 v44, v41, v21
	v_dot4c_i32_i8_e32 v40, v37, v21
	v_dot4c_i32_i8_e32 v36, v33, v21
	v_dot4c_i32_i8_e32 v32, v29, v21
	v_dot4c_i32_i8_e32 v28, v25, v21
	v_cndmask_b32_e32 v20, v96, v56, vcc
	v_cndmask_b32_e32 v21, v56, v96, vcc
	v_dot4c_i32_i8_e32 v80, v79, v23
	v_dot4c_i32_i8_e32 v76, v74, v22
	v_dot4c_i32_i8_e32 v72, v70, v22
	v_dot4c_i32_i8_e32 v68, v66, v22
	v_dot4c_i32_i8_e32 v64, v62, v22
	v_dot4c_i32_i8_e32 v60, v58, v22
	v_dot4c_i32_i8_e32 v48, v47, v23
	v_dot4c_i32_i8_e32 v44, v42, v22
	v_dot4c_i32_i8_e32 v40, v38, v22
	v_dot4c_i32_i8_e32 v36, v34, v22
	v_dot4c_i32_i8_e32 v32, v30, v22
	v_dot4c_i32_i8_e32 v28, v26, v22
	v_add_u32_dpp v20, v20, v21 row_half_mirror row_mask:0xf bank_mask:0xf bound_ctrl:1
	v_cndmask_b32_e32 v21, v84, v52, vcc
	v_cndmask_b32_e32 v22, v52, v84, vcc
	v_dot4c_i32_i8_e32 v76, v75, v23
	v_dot4c_i32_i8_e32 v72, v71, v23
	v_dot4c_i32_i8_e32 v68, v67, v23
	v_dot4c_i32_i8_e32 v64, v63, v23
	v_dot4c_i32_i8_e32 v60, v59, v23
	v_dot4c_i32_i8_e32 v44, v43, v23
	v_dot4c_i32_i8_e32 v40, v39, v23
	v_dot4c_i32_i8_e32 v36, v35, v23
	v_dot4c_i32_i8_e32 v32, v31, v23
	v_dot4c_i32_i8_e32 v28, v27, v23
	v_add_u32_dpp v21, v21, v22 row_half_mirror row_mask:0xf bank_mask:0xf bound_ctrl:1
	v_cndmask_b32_e32 v22, v80, v48, vcc
	v_cndmask_b32_e32 v23, v48, v80, vcc
	v_cndmask_b32_e32 v24, v44, v76, vcc
	v_cndmask_b32_e32 v25, v40, v72, vcc
	v_add_u32_dpp v22, v22, v23 row_half_mirror row_mask:0xf bank_mask:0xf bound_ctrl:1
	v_cndmask_b32_e32 v23, v76, v44, vcc
	v_cndmask_b32_e32 v26, v36, v68, vcc
	v_cndmask_b32_e32 v27, v32, v64, vcc
	v_add_u32_dpp v23, v23, v24 row_half_mirror row_mask:0xf bank_mask:0xf bound_ctrl:1
	v_cndmask_b32_e32 v24, v72, v40, vcc
	s_nop 1
	v_add_u32_dpp v24, v24, v25 row_half_mirror row_mask:0xf bank_mask:0xf bound_ctrl:1
	v_cndmask_b32_e32 v25, v68, v36, vcc
	s_nop 1
	v_add_u32_dpp v25, v25, v26 row_half_mirror row_mask:0xf bank_mask:0xf bound_ctrl:1
	v_cndmask_b32_e32 v26, v64, v32, vcc
	s_nop 1
	v_add_u32_dpp v26, v26, v27 row_half_mirror row_mask:0xf bank_mask:0xf bound_ctrl:1
	v_cndmask_b32_e32 v27, v60, v28, vcc
	v_cndmask_b32_e32 v28, v28, v60, vcc
	s_nop 1
	v_add_u32_dpp v27, v27, v28 row_half_mirror row_mask:0xf bank_mask:0xf bound_ctrl:1
	v_and_b32_e32 v28, 2, v94
	v_cmp_eq_u32_e32 vcc, 0, v28
	s_nop 1
	v_cndmask_b32_e32 v28, v20, v24, vcc
	v_cndmask_b32_e32 v20, v24, v20, vcc
	v_cndmask_b32_e32 v24, v21, v25, vcc
	v_cndmask_b32_e32 v21, v25, v21, vcc
	v_add_u32_dpp v20, v28, v20 quad_perm:[2,3,0,1] row_mask:0xf bank_mask:0xf bound_ctrl:1
	s_nop 0
	v_add_u32_dpp v21, v24, v21 quad_perm:[2,3,0,1] row_mask:0xf bank_mask:0xf bound_ctrl:1
	v_cndmask_b32_e32 v24, v22, v26, vcc
	v_cndmask_b32_e32 v22, v26, v22, vcc
	s_nop 1
	v_add_u32_dpp v22, v24, v22 quad_perm:[2,3,0,1] row_mask:0xf bank_mask:0xf bound_ctrl:1
	v_cndmask_b32_e32 v24, v23, v27, vcc
	v_cndmask_b32_e32 v23, v27, v23, vcc
	s_nop 1
	v_add_u32_dpp v23, v24, v23 quad_perm:[2,3,0,1] row_mask:0xf bank_mask:0xf bound_ctrl:1
	v_and_b32_e32 v24, 1, v94
	v_cmp_eq_u32_e32 vcc, 0, v24
	s_nop 1
	v_cndmask_b32_e32 v24, v20, v22, vcc
	v_cndmask_b32_e32 v20, v22, v20, vcc
	v_cndmask_b32_e32 v22, v21, v23, vcc
	v_cndmask_b32_e32 v21, v23, v21, vcc
	v_add_u32_dpp v20, v24, v20 quad_perm:[1,0,3,2] row_mask:0xf bank_mask:0xf bound_ctrl:1
	v_mov_b32_e32 v24, 0
	v_add_u32_dpp v21, v22, v21 quad_perm:[1,0,3,2] row_mask:0xf bank_mask:0xf bound_ctrl:1
	v_and_b32_e32 v22, 1, v95
	v_cmp_eq_u32_e32 vcc, 0, v22
	v_lshlrev_b32_e32 v22, 4, v22
	v_lshl_or_b32 v200, v93, 5, v22
	v_cndmask_b32_e32 v23, v20, v21, vcc
	s_nop 1
	v_mov_b32_dpp v24, v23 row_ror:8 row_mask:0xf bank_mask:0xf
	v_cndmask_b32_e32 v20, v24, v20, vcc
	v_cndmask_b32_e32 v21, v21, v24, vcc
	v_add_u32_e32 v20, 32, v20
	v_lshrrev_b32_e32 v20, 6, v20
	v_lshl_add_u32 v21, v21, 10, v239
	v_bfi_b32 v23, s27, v20, v21
	v_ashrrev_i32_e32 v20, 4, v94
	v_ashrrev_i32_e32 v21, 31, v20
	v_lshl_add_u64 v[20:21], v[20:21], 2, v[200:201]
	v_lshl_add_u64 v[20:21], s[14:15], 0, v[20:21]
	global_store_dword v[20:21], v23, off
	s_waitcnt lgkmcnt(0)
	s_add_u32 s14, s14, 0x100
	s_addc_u32 s15, s15, 0
	s_cmp_eq_u32 s26, s46
	s_cbranch_scc0 .LBB0_1995
	s_and_b64 vcc, exec, s[6:7]
	s_mov_b32 s26, s21
	s_mov_b32 s23, s22
	s_cbranch_vccz .LBB0_1982

.LBB0_2163:
	v_readfirstlane_b32 s13, v95
	s_lshr_b32 s6, s32, 15
	s_add_i32 s13, s13, s6
	s_cmpk_lt_u32 s13, 0x1100
	s_cbranch_scc1 .LBB0_2170
	s_add_i32 s6, s18, s15
	s_lshl_b32 s10, s6, 6
	s_branch .LBB0_2167

.LBB0_2175:
	s_lshl_b32 s13, s23, 3
	s_and_b32 s13, s13, 0x3ff8
	s_lshr_b32 s9, s23, 11
	s_lshl_b32 s8, s23, 2
	s_add_i32 s8, s8, 0xfffffc00
	s_cmp_ge_u32 s23, 0xf00
	s_cselect_b32 s13, s8, s13
	s_cselect_b32 s9, 1, s9
	s_cselect_b32 s46, 4, 8
	s_add_i32 s45, s46, -2
	s_lshl_b32 s8, s12, 1
	s_add_i32 s94, s8, s9
	s_xor_b64 s[6:7], s[10:11], -1
	s_lshl_b64 s[8:9], s[94:95], 21
	s_add_u32 s8, s16, s8
	s_addc_u32 s9, s17, s9
	s_lshl_b32 s12, s19, 3
	s_and_b32 s12, s12, 0x3ff8
	s_lshl_b32 s44, s19, 2
	s_add_i32 s44, s44, 0xfffffc00
	s_cmp_ge_u32 s19, 0xf00
	s_cselect_b32 s12, s44, s12
	s_and_b64 s[10:11], s[10:11], exec
	s_cselect_b32 s22, s12, s13
	s_lshl_b32 s10, s94, 7
	s_or_b32 s21, s13, 2
	s_sub_i32 s22, s22, s45
	s_lshl_b32 s23, s13, 2
	s_lshl_b32 s11, s13, 11
	s_add_u32 s10, s11, s10
	s_addc_u32 s11, 0, 0
	s_lshl_b32 s25, s13, 7
	s_lshl_b64 s[12:13], s[94:95], 2
	s_add_u32 s25, s25, s12
	s_mov_b32 s24, s95
	s_addc_u32 s26, 0, s13
	s_mov_b32 s27, 0
	s_branch .LBB0_2177
.LBB0_2176:
	s_or_b64 exec, exec, s[12:13]
	s_add_i32 s27, s27, 1
	s_add_u32 s23, s23, 4
	s_addc_u32 s24, s24, 0
	s_add_u32 s10, s10, 0x800
	s_addc_u32 s11, s11, 0
	s_add_u32 s25, s25, 0x80
	s_waitcnt lgkmcnt(0)
	s_addc_u32 s26, s26, 0
	s_cmp_eq_u32 s27, s46
	s_cbranch_scc1 .LBB0_2162
.LBB0_2177:
	s_waitcnt lgkmcnt(0)
	v_mov_b64_e32 v[22:23], v[18:19]
	v_mov_b32_e32 v97, v94
	v_mov_b64_e32 v[20:21], v[16:17]
	s_nop 0
	v_lshlrev_b32_e32 v16, 4, v97
	v_and_b32_e32 v200, 0x70, v16
	v_add_u32_e32 v12, v200, v12
	v_add_u32_e32 v8, v200, v8
	global_load_dwordx4 v[72:75], v12, s[8:9]
	global_load_dwordx4 v[56:59], v8, s[8:9]
	v_add_u32_e32 v12, v200, v13
	v_add_u32_e32 v8, v200, v9
	global_load_dwordx4 v[76:79], v12, s[8:9]
	global_load_dwordx4 v[60:63], v8, s[8:9]
	v_add_u32_e32 v12, v200, v14
	v_add_u32_e32 v8, v200, v10
	global_load_dwordx4 v[80:83], v12, s[8:9]
	global_load_dwordx4 v[64:67], v8, s[8:9]
	v_add_u32_e32 v12, v200, v15
	global_load_dwordx4 v[84:87], v12, s[8:9]
	v_add_u32_e32 v8, v200, v11
	global_load_dwordx4 v[68:71], v8, s[8:9]
	v_add_u32_e32 v4, v200, v4
	v_add_u32_e32 v0, v200, v0
	global_load_dwordx4 v[40:43], v4, s[8:9]
	global_load_dwordx4 v[24:27], v0, s[8:9]
	v_add_u32_e32 v4, v200, v5
	v_add_u32_e32 v0, v200, v1
	global_load_dwordx4 v[44:47], v4, s[8:9]
	global_load_dwordx4 v[28:31], v0, s[8:9]
	v_add_u32_e32 v4, v200, v6
	v_add_u32_e32 v0, v200, v2
	global_load_dwordx4 v[48:51], v4, s[8:9]
	global_load_dwordx4 v[32:35], v0, s[8:9]
	v_add_u32_e32 v4, v200, v7
	global_load_dwordx4 v[52:55], v4, s[8:9]
	v_add_u32_e32 v0, v200, v3
	global_load_dwordx4 v[36:39], v0, s[8:9]
	v_ashrrev_i32_e32 v18, 3, v97
	v_lshlrev_b32_e32 v16, 1, v18
	v_ashrrev_i32_e32 v17, 31, v16
	v_lshl_add_u32 v0, v97, 3, s84
	v_lshl_add_u64 v[16:17], v[200:201], 0, v[16:17]
	s_waitcnt vmcnt(17)
	ds_write_b64 v0, v[88:89]
	v_mad_u64_u32 v[0:1], s[12:13], v97, -6, v[0:1]
	v_lshl_add_u64 v[90:91], s[10:11], 0, v[16:17]
	s_waitcnt vmcnt(16)
	ds_write_b16 v0, v96 offset:512
	s_waitcnt lgkmcnt(0)
	v_lshl_add_u32 v0, v18, 6, s84
	v_lshl_add_u64 v[92:93], v[90:91], 1, s[70:71]
	ds_read_b128 v[12:15], v0
	ds_read_b128 v[8:11], v0 offset:16
	ds_read_b128 v[4:7], v0 offset:32
	ds_read_b128 v[0:3], v0 offset:48
	global_load_dword v98, v[92:93], off
	s_add_u32 s12, s92, s23
	v_lshl_add_u32 v16, v18, 4, s84
	s_addc_u32 s13, s93, s24
	ds_read_b128 v[16:19], v16 offset:512
	global_load_dword v100, v231, s[12:13]
	global_load_dword v99, v232, s[12:13]
	s_cmp_lt_u32 s27, s45
	s_cselect_b32 s12, s21, s22
	s_add_i32 s12, s12, s27
	s_ashr_i32 s13, s12, 31
	s_lshl_b64 s[28:29], s[12:13], 7
	s_lshl_b64 s[12:13], s[12:13], 9
	v_lshlrev_b32_e32 v102, 1, v97
	s_add_u32 s12, s82, s12
	s_addc_u32 s13, s83, s13
	v_ashrrev_i32_e32 v103, 31, v102
	v_lshl_add_u64 v[88:89], v[102:103], 2, s[12:13]
	s_add_u32 s12, s56, s28
	s_addc_u32 s13, s57, s29
	v_lshl_add_u64 v[102:103], s[12:13], 0, v[102:103]
	global_load_dwordx2 v[88:89], v[88:89], off
	s_mov_b32 s12, 0x6050400
	global_load_ushort v96, v[102:103], off
	s_waitcnt vmcnt(18)
	v_perm_b32 v101, v76, v72, s89
	v_perm_b32 v72, v76, v72, s86
	s_waitcnt vmcnt(14)
	v_perm_b32 v76, v84, v80, s89
	v_perm_b32 v80, v84, v80, s86
	v_perm_b32 v84, v76, v101, s87
	v_perm_b32 v76, v76, v101, s72
	v_perm_b32 v101, v80, v72, s87
	v_perm_b32 v80, v80, v72, s72
	v_mov_b32_e32 v72, v201
	v_dot4c_i32_i8_e32 v72, v84, v20
	v_mov_b32_e32 v84, v201
	v_dot4c_i32_i8_e32 v84, v76, v20
	v_mov_b32_e32 v76, v201
	v_dot4c_i32_i8_e32 v76, v101, v20
	v_mov_b32_e32 v101, v201
	v_dot4c_i32_i8_e32 v101, v80, v20
	v_perm_b32 v80, v77, v73, s89
	v_perm_b32 v73, v77, v73, s86
	v_perm_b32 v77, v85, v81, s89
	v_perm_b32 v81, v85, v81, s86
	v_perm_b32 v85, v77, v80, s87
	v_perm_b32 v77, v77, v80, s72
	v_perm_b32 v80, v81, v73, s87
	v_perm_b32 v73, v81, v73, s72
	v_mov_b32_e32 v81, v201
	v_dot4c_i32_i8_e32 v81, v85, v20
	v_mov_b32_e32 v85, v201
	v_dot4c_i32_i8_e32 v85, v77, v20
	v_mov_b32_e32 v77, v201
	v_dot4c_i32_i8_e32 v77, v80, v20
	v_mov_b32_e32 v80, v201
	v_dot4c_i32_i8_e32 v80, v73, v20
	v_perm_b32 v73, v78, v74, s89
	v_perm_b32 v74, v78, v74, s86
	v_perm_b32 v78, v86, v82, s89
	v_perm_b32 v82, v86, v82, s86
	v_perm_b32 v86, v78, v73, s87
	v_perm_b32 v73, v78, v73, s72
	v_perm_b32 v78, v82, v74, s87
	v_perm_b32 v74, v82, v74, s72
	v_mov_b32_e32 v82, v201
	v_dot4c_i32_i8_e32 v82, v86, v20
	v_mov_b32_e32 v86, v201
	v_dot4c_i32_i8_e32 v86, v73, v20
	v_mov_b32_e32 v73, v201
	v_dot4c_i32_i8_e32 v73, v78, v20
	v_mov_b32_e32 v78, v201
	v_dot4c_i32_i8_e32 v78, v74, v20
	v_perm_b32 v74, v79, v75, s89
	v_perm_b32 v75, v79, v75, s86
	v_perm_b32 v79, v87, v83, s89
	v_perm_b32 v83, v87, v83, s86
	v_perm_b32 v87, v79, v74, s87
	v_perm_b32 v74, v79, v74, s72
	v_perm_b32 v79, v83, v75, s87
	v_perm_b32 v75, v83, v75, s72
	v_mov_b32_e32 v83, v201
	v_dot4c_i32_i8_e32 v83, v87, v20
	v_mov_b32_e32 v87, v201
	v_dot4c_i32_i8_e32 v87, v74, v20
	v_mov_b32_e32 v74, v201
	v_dot4c_i32_i8_e32 v74, v79, v20
	v_mov_b32_e32 v79, v201
	v_dot4c_i32_i8_e32 v79, v75, v20
	v_perm_b32 v20, v60, v56, s89
	v_perm_b32 v56, v60, v56, s86
	s_waitcnt vmcnt(13)
	v_perm_b32 v60, v68, v64, s89
	v_perm_b32 v64, v68, v64, s86
	v_perm_b32 v68, v60, v20, s87
	v_perm_b32 v20, v60, v20, s72
	v_perm_b32 v60, v64, v56, s87
	v_perm_b32 v56, v64, v56, s72
	v_dot4c_i32_i8_e32 v84, v20, v21
	v_dot4c_i32_i8_e32 v76, v60, v21
	v_dot4c_i32_i8_e32 v101, v56, v21
	v_perm_b32 v20, v61, v57, s89
	v_perm_b32 v56, v61, v57, s86
	v_perm_b32 v57, v69, v65, s89
	v_perm_b32 v60, v69, v65, s86
	v_perm_b32 v61, v57, v20, s87
	v_perm_b32 v20, v57, v20, s72
	v_perm_b32 v57, v60, v56, s87
	v_perm_b32 v56, v60, v56, s72
	v_dot4c_i32_i8_e32 v85, v20, v21
	v_dot4c_i32_i8_e32 v77, v57, v21
	v_dot4c_i32_i8_e32 v80, v56, v21
	v_perm_b32 v20, v62, v58, s89
	v_perm_b32 v56, v62, v58, s86
	v_perm_b32 v57, v70, v66, s89
	v_perm_b32 v58, v70, v66, s86
	v_perm_b32 v60, v57, v20, s87
	v_perm_b32 v20, v57, v20, s72
	v_perm_b32 v57, v58, v56, s87
	v_perm_b32 v56, v58, v56, s72
	v_dot4c_i32_i8_e32 v86, v20, v21
	v_dot4c_i32_i8_e32 v73, v57, v21
	v_dot4c_i32_i8_e32 v78, v56, v21
	v_perm_b32 v20, v63, v59, s89
	v_perm_b32 v56, v63, v59, s86
	v_perm_b32 v57, v71, v67, s89
	v_perm_b32 v58, v71, v67, s86
	v_perm_b32 v59, v57, v20, s87
	v_perm_b32 v20, v57, v20, s72
	v_perm_b32 v57, v58, v56, s87
	v_perm_b32 v56, v58, v56, s72
	v_dot4c_i32_i8_e32 v72, v68, v21
	v_dot4c_i32_i8_e32 v81, v61, v21
	v_dot4c_i32_i8_e32 v82, v60, v21
	v_dot4c_i32_i8_e32 v83, v59, v21
	v_dot4c_i32_i8_e32 v87, v20, v21
	v_dot4c_i32_i8_e32 v74, v57, v21
	v_dot4c_i32_i8_e32 v79, v56, v21
	s_waitcnt vmcnt(10)
	v_perm_b32 v20, v44, v40, s89
	v_perm_b32 v21, v44, v40, s86
	s_waitcnt vmcnt(6)
	v_perm_b32 v40, v52, v48, s89
	v_perm_b32 v44, v52, v48, s86
	v_perm_b32 v48, v40, v20, s87
	v_perm_b32 v20, v40, v20, s72
	v_perm_b32 v40, v44, v21, s87
	v_perm_b32 v21, v44, v21, s72
	v_dot4c_i32_i8_e32 v84, v20, v22
	v_dot4c_i32_i8_e32 v76, v40, v22
	v_dot4c_i32_i8_e32 v101, v21, v22
	v_perm_b32 v20, v45, v41, s89
	v_perm_b32 v21, v45, v41, s86
	v_perm_b32 v40, v53, v49, s89
	v_perm_b32 v41, v53, v49, s86
	v_perm_b32 v44, v40, v20, s87
	v_perm_b32 v20, v40, v20, s72
	v_perm_b32 v40, v41, v21, s87
	v_perm_b32 v21, v41, v21, s72
	v_dot4c_i32_i8_e32 v85, v20, v22
	v_dot4c_i32_i8_e32 v77, v40, v22
	v_dot4c_i32_i8_e32 v80, v21, v22
	v_perm_b32 v20, v46, v42, s89
	v_perm_b32 v21, v46, v42, s86
	v_perm_b32 v40, v54, v50, s89
	v_perm_b32 v41, v54, v50, s86
	v_perm_b32 v42, v40, v20, s87
	v_perm_b32 v20, v40, v20, s72
	v_perm_b32 v40, v41, v21, s87
	v_perm_b32 v21, v41, v21, s72
	v_dot4c_i32_i8_e32 v86, v20, v22
	v_dot4c_i32_i8_e32 v73, v40, v22
	v_dot4c_i32_i8_e32 v78, v21, v22
	v_perm_b32 v20, v47, v43, s89
	v_perm_b32 v21, v47, v43, s86
	v_perm_b32 v40, v55, v51, s89
	v_perm_b32 v41, v55, v51, s86
	v_dot4c_i32_i8_e32 v82, v42, v22
	v_perm_b32 v42, v40, v20, s87
	v_perm_b32 v20, v40, v20, s72
	v_perm_b32 v40, v41, v21, s87
	v_perm_b32 v21, v41, v21, s72
	v_dot4c_i32_i8_e32 v72, v48, v22
	v_dot4c_i32_i8_e32 v81, v44, v22
	v_dot4c_i32_i8_e32 v83, v42, v22
	v_dot4c_i32_i8_e32 v87, v20, v22
	v_dot4c_i32_i8_e32 v74, v40, v22
	v_dot4c_i32_i8_e32 v79, v21, v22
	v_perm_b32 v20, v28, v24, s89
	v_perm_b32 v21, v28, v24, s86
	s_waitcnt vmcnt(5)
	v_perm_b32 v22, v36, v32, s89
	v_perm_b32 v24, v36, v32, s86
	v_perm_b32 v28, v22, v20, s87
	v_perm_b32 v20, v22, v20, s72
	v_perm_b32 v22, v24, v21, s87
	v_perm_b32 v21, v24, v21, s72
	v_dot4c_i32_i8_e32 v84, v20, v23
	v_dot4c_i32_i8_e32 v76, v22, v23
	v_dot4c_i32_i8_e32 v101, v21, v23
	v_perm_b32 v20, v29, v25, s89
	v_perm_b32 v21, v29, v25, s86
	v_perm_b32 v22, v37, v33, s89
	v_perm_b32 v24, v37, v33, s86
	v_perm_b32 v25, v22, v20, s87
	v_perm_b32 v20, v22, v20, s72
	v_perm_b32 v22, v24, v21, s87
	v_perm_b32 v21, v24, v21, s72
	v_dot4c_i32_i8_e32 v85, v20, v23
	v_dot4c_i32_i8_e32 v77, v22, v23
	v_dot4c_i32_i8_e32 v80, v21, v23
	v_perm_b32 v20, v30, v26, s89
	v_perm_b32 v21, v30, v26, s86
	v_perm_b32 v22, v38, v34, s89
	v_perm_b32 v24, v38, v34, s86
	v_dot4c_i32_i8_e32 v81, v25, v23
	v_perm_b32 v25, v22, v20, s87
	v_perm_b32 v20, v22, v20, s72
	v_perm_b32 v22, v24, v21, s87
	v_perm_b32 v21, v24, v21, s72
	v_dot4c_i32_i8_e32 v86, v20, v23
	v_dot4c_i32_i8_e32 v73, v22, v23
	v_perm_b32 v20, v31, v27, s89
	v_perm_b32 v22, v39, v35, s89
	v_dot4c_i32_i8_e32 v82, v25, v23
	v_dot4c_i32_i8_e32 v78, v21, v23
	v_perm_b32 v21, v31, v27, s86
	v_perm_b32 v24, v39, v35, s86
	v_perm_b32 v25, v22, v20, s87
	v_dot4c_i32_i8_e32 v72, v28, v23
	v_perm_b32 v20, v22, v20, s72
	v_perm_b32 v22, v24, v21, s87
	v_dot4c_i32_i8_e32 v83, v25, v23
	v_dot4c_i32_i8_e32 v74, v22, v23
	v_permlane32_swap_b32_e32 v72, v82
	s_nop 0
	v_permlane32_swap_b32_e32 v81, v83
	v_perm_b32 v21, v24, v21, s72
	v_dot4c_i32_i8_e32 v87, v20, v23
	v_add_u32_e32 v20, v72, v82
	v_permlane32_swap_b32_e32 v76, v73
	v_add_u32_e32 v24, v81, v83
	v_permlane32_swap_b32_e32 v77, v74
	v_add_u32_e32 v22, v76, v73
	v_add_u32_e32 v26, v77, v74
	v_permlane16_swap_b32_e32 v20, v24
	v_add_u32_e32 v20, v20, v24
	v_permlane16_swap_b32_e32 v22, v26
	v_and_b32_e32 v24, 8, v97
	v_dot4c_i32_i8_e32 v79, v21, v23
	v_add_u32_e32 v22, v22, v26
	v_cmp_eq_u32_e32 vcc, 0, v24
	v_permlane32_swap_b32_e32 v84, v86
	v_permlane32_swap_b32_e32 v101, v78
	v_permlane32_swap_b32_e32 v85, v87
	v_permlane32_swap_b32_e32 v80, v79
	v_cndmask_b32_e32 v24, v20, v22, vcc
	v_cndmask_b32_e32 v20, v22, v20, vcc
	v_add_u32_e32 v21, v84, v86
	v_add_u32_e32 v23, v101, v78
	v_add_u32_e32 v25, v85, v87
	v_add_u32_e32 v27, v80, v79
	v_add_u32_dpp v20, v24, v20 row_ror:8 row_mask:0xf bank_mask:0xf bound_ctrl:1
	v_permlane16_swap_b32_e32 v21, v25
	v_permlane16_swap_b32_e32 v23, v27
	v_cvt_f32_i32_e32 v20, v20
	v_add_u32_e32 v21, v21, v25
	v_add_u32_e32 v23, v23, v27
	v_cndmask_b32_e32 v22, v21, v23, vcc
	v_cndmask_b32_e32 v21, v23, v21, vcc
	s_waitcnt vmcnt(4)
	v_and_b32_e32 v23, 0xffff0000, v98
	v_add_u32_dpp v21, v22, v21 row_ror:8 row_mask:0xf bank_mask:0xf bound_ctrl:1
	v_lshlrev_b32_e32 v22, 16, v98
	s_waitcnt vmcnt(3)
	v_fmac_f32_e32 v22, v100, v20
	v_cvt_f32_i32_e32 v20, v21
	v_fmac_f32_e32 v23, v100, v20
	v_cvt_pk_bf16_f32 v20, v22, v23
	global_store_dword v[92:93], v20, off
	s_waitcnt vmcnt(3)
	v_mul_f32_e32 v20, v99, v22
	v_mul_f32_e32 v21, v99, v23
	v_rndne_f32_e32 v20, v20
	v_rndne_f32_e32 v21, v21
	v_med3_f32 v20, v20, s88, v236
	v_med3_f32 v21, v21, s88, v236
	v_cvt_i32_f32_e32 v20, v20
	v_cvt_i32_f32_e32 v21, v21
	v_perm_b32 v24, v21, v20, s12
	v_lshl_add_u64 v[20:21], s[92:93], 0, v[90:91]
	s_mov_b32 s12, 0x46200000
	v_add_co_u32_e32 v20, vcc, s12, v20
	s_nop 1
	v_addc_co_u32_e32 v21, vcc, 0, v21, vcc
	global_store_short v[20:21], v24, off
	v_mul_f32_e32 v20, v23, v23
	v_fmac_f32_e32 v20, v22, v22
	v_cmp_eq_u32_e32 vcc, 0, v97
	s_nop 0
	v_add_f32_dpp v20, v20, v20 row_ror:1 row_mask:0xf bank_mask:0xf bound_ctrl:1
	s_nop 1
	v_add_f32_dpp v20, v20, v20 row_ror:2 row_mask:0xf bank_mask:0xf bound_ctrl:1
	s_nop 1
	v_add_f32_dpp v20, v20, v20 row_ror:4 row_mask:0xf bank_mask:0xf bound_ctrl:1
	s_nop 1
	v_add_f32_dpp v20, v20, v20 row_ror:8 row_mask:0xf bank_mask:0xf bound_ctrl:1
	s_nop 0
	v_readlane_b32 s28, v20, 16
	v_readlane_b32 s29, v20, 32
	v_readlane_b32 s30, v20, 48
	s_and_saveexec_b64 s[12:13], vcc
	s_cbranch_execz .LBB0_2176
	v_add_f32_e32 v20, s28, v20
	s_add_u32 s34, s92, s25
	v_add_f32_e32 v20, s29, v20
	s_addc_u32 s35, s93, s26
	v_add_f32_e32 v20, s30, v20
	global_store_dword v233, v20, s[34:35]
	global_store_dword v233, v201, s[34:35] offset:64
	s_branch .LBB0_2176
